# v52 + k_agg2 epilogue de-serialised: pointer kernargs fetched at the top, b2 bias requested before the reduction
# speedup vs baseline: 1.0044x; 1.0002x over previous
_Z6k_agg2PKDv4_jPKiS3_PK15HIP_vector_typeIiLj2EEPKfPfSA_PS_:
	s_load_dwordx4 s[8:11], s[0:1], 0x0
	s_load_dwordx2 s[4:5], s[0:1], 0x10
	s_load_dwordx2 s[12:13], s[0:1], 0x20
	s_load_dwordx2 s[14:15], s[0:1], 0x28
	s_load_dwordx4 s[16:19], s[0:1], 0x30
	v_lshrrev_b32_e32 v1, 6, v0
	v_lshl_or_b32 v24, s2, 2, v1
	v_ashrrev_i32_e32 v25, 31, v24
	v_and_b32_e32 v41, 63, v0
	s_waitcnt lgkmcnt(0)
	v_lshl_add_u64 v[2:3], v[24:25], 2, s[4:5]
	global_load_dword v45, v[2:3], off
	v_lshl_or_b32 v2, v24, 6, v41
	v_ashrrev_i32_e32 v3, 31, v2
	v_lshl_add_u64 v[2:3], v[2:3], 2, s[10:11]
	global_load_dword v8, v[2:3], off
	v_lshlrev_b32_e32 v1, 8, v0
	v_and_b32_e32 v28, 0x2000, v1
	v_mov_b32_e32 v29, 0
	v_and_b32_e32 v43, 7, v0
	v_lshlrev_b32_e32 v2, 7, v28
	v_mov_b32_e32 v3, v29
	v_lshl_add_u64 v[2:3], s[8:9], 0, v[2:3]
	v_lshlrev_b32_e32 v26, 4, v43
	v_mov_b32_e32 v27, v29
	v_bfe_u32 v9, v0, 3, 2
	v_lshl_add_u64 v[30:31], v[2:3], 0, v[26:27]
	v_cmp_eq_u32_e32 vcc, 0, v9
	v_mov_b32_e32 v6, 0
	v_mov_b32_e32 v7, 0
	v_mov_b32_e32 v4, 0
	v_mov_b32_e32 v5, 0
	v_mov_b32_e32 v2, 0
	v_mov_b32_e32 v3, 0
	v_mov_b32_e32 v0, 0
	v_mov_b32_e32 v1, 0
	s_and_saveexec_b64 s[2:3], vcc
	s_cbranch_execz .LBB3_2
	v_lshlrev_b64 v[0:1], 7, v[24:25]
	v_lshl_add_u64 v[0:1], v[30:31], 0, v[0:1]
	global_load_dwordx4 v[0:3], v[0:1], off
	s_waitcnt vmcnt(0)
	v_cvt_f32_f16_e32 v6, v0
	v_cvt_f32_f16_e32 v4, v1
	v_cvt_f32_f16_e32 v10, v2
	v_cvt_f32_f16_e32 v12, v3
	v_cvt_f32_f16_sdwa v13, v3 dst_sel:DWORD dst_unused:UNUSED_PAD src0_sel:WORD_1
	v_cvt_f32_f16_sdwa v11, v2 dst_sel:DWORD dst_unused:UNUSED_PAD src0_sel:WORD_1
	v_cvt_f32_f16_sdwa v5, v1 dst_sel:DWORD dst_unused:UNUSED_PAD src0_sel:WORD_1
	v_cvt_f32_f16_sdwa v7, v0 dst_sel:DWORD dst_unused:UNUSED_PAD src0_sel:WORD_1
	v_pk_add_f32 v[0:1], v[12:13], 0 op_sel_hi:[1,0]
	v_pk_add_f32 v[2:3], v[10:11], 0 op_sel_hi:[1,0]
	v_pk_add_f32 v[4:5], v[4:5], 0 op_sel_hi:[1,0]
	v_pk_add_f32 v[6:7], v[6:7], 0 op_sel_hi:[1,0]

.LBB3_10:
	s_or_b64 exec, exec, s[6:7]
	v_lshlrev_b32_e32 v60, 5, v43
	global_load_dwordx4 v[52:55], v60, s[12:13]
	global_load_dwordx4 v[56:59], v60, s[12:13] offset:16
	v_and_b32_e32 v1, 64, v27
	v_xor_b32_e32 v0, 8, v27
	v_add_u32_e32 v2, 64, v1
	v_cmp_lt_i32_e64 s[2:3], v0, v2
	v_xor_b32_e32 v3, 16, v27
	s_nop 0
	v_cndmask_b32_e64 v0, v27, v0, s[2:3]
	v_lshlrev_b32_e32 v7, 2, v0
	v_cmp_lt_i32_e64 s[2:3], v3, v2
	ds_bpermute_b32 v0, v7, v36
	ds_bpermute_b32 v1, v7, v37
	v_cndmask_b32_e64 v4, v27, v3, s[2:3]
	ds_bpermute_b32 v2, v7, v38
	ds_bpermute_b32 v3, v7, v39
	ds_bpermute_b32 v8, v7, v32
	ds_bpermute_b32 v9, v7, v33
	ds_bpermute_b32 v10, v7, v34
	ds_bpermute_b32 v11, v7, v35
	v_lshlrev_b32_e32 v13, 2, v4
	s_waitcnt lgkmcnt(6)
	v_pk_add_f32 v[0:1], v[36:37], v[0:1]
	s_waitcnt lgkmcnt(4)
	v_pk_add_f32 v[2:3], v[38:39], v[2:3]
	s_waitcnt lgkmcnt(2)
	v_pk_add_f32 v[14:15], v[32:33], v[8:9]
	s_waitcnt lgkmcnt(0)
	v_pk_add_f32 v[10:11], v[34:35], v[10:11]
	ds_bpermute_b32 v4, v13, v0
	ds_bpermute_b32 v5, v13, v1
	ds_bpermute_b32 v6, v13, v2
	ds_bpermute_b32 v7, v13, v3
	ds_bpermute_b32 v16, v13, v14
	ds_bpermute_b32 v17, v13, v15
	ds_bpermute_b32 v12, v13, v10
	ds_bpermute_b32 v13, v13, v11
	s_and_saveexec_b64 s[2:3], vcc
	s_cbranch_execz .LBB3_13
	s_mov_b64 s[4:5], s[16:17]
	s_mov_b64 s[6:7], s[18:19]
	v_lshlrev_b32_e32 v8, 5, v43
	v_add_u32_e32 v22, 1, v45
	s_waitcnt lgkmcnt(0)
	v_pk_add_f32 v[10:11], v[10:11], v[12:13]
	v_cvt_f32_i32_e32 v12, v22
	s_mov_b32 s2, 0xf800000
	v_pk_add_f32 v[0:1], v[0:1], v[4:5]
	v_lshl_add_u64 v[4:5], v[28:29], 0, v[24:25]
	v_mul_f32_e32 v13, 0x4f800000, v12
	v_cmp_gt_f32_e32 vcc, s2, v12
	v_pk_add_f32 v[2:3], v[2:3], v[6:7]
	v_lshlrev_b64 v[6:7], 8, v[4:5]
	v_cndmask_b32_e32 v12, v12, v13, vcc
	v_sqrt_f32_e32 v13, v12
	v_mov_b32_e32 v9, 0
	v_lshl_add_u64 v[6:7], s[4:5], 0, v[6:7]
	v_pk_add_f32 v[14:15], v[14:15], v[16:17]
	v_lshl_add_u64 v[16:17], v[6:7], 0, v[8:9]
	v_add_u32_e32 v6, -1, v13
	v_add_u32_e32 v7, 1, v13
	v_fma_f32 v8, -v6, v13, v12
	v_fma_f32 v22, -v7, v13, v12
	v_cmp_ge_f32_e64 s[2:3], 0, v8
	v_mov_b32_e32 v23, 0x260
	v_lshlrev_b64 v[4:5], 7, v[4:5]
	v_cndmask_b32_e64 v6, v13, v6, s[2:3]
	v_cmp_lt_f32_e64 s[2:3], 0, v22
	v_mov_b32_e32 v27, v9
	v_lshl_add_u64 v[4:5], s[6:7], 0, v[4:5]
	v_cndmask_b32_e64 v6, v6, v7, s[2:3]
	v_mul_f32_e32 v7, 0x37800000, v6
	v_cndmask_b32_e32 v6, v6, v7, vcc
	v_cmp_class_f32_e32 vcc, v12, v23
	v_lshl_add_u64 v[22:23], v[4:5], 0, v[26:27]
	s_nop 0
	v_cndmask_b32_e32 v6, v6, v12, vcc
	v_div_scale_f32 v7, s[2:3], v6, v6, 1.0
	v_rcp_f32_e32 v8, v7
	v_div_scale_f32 v4, vcc, 1.0, v6, 1.0
	v_fma_f32 v5, -v7, v8, 1.0
	v_fmac_f32_e32 v8, v5, v8
	v_mul_f32_e32 v5, v4, v8
	v_fma_f32 v12, -v7, v5, v4
	v_fmac_f32_e32 v5, v12, v8
	v_fma_f32 v4, -v7, v5, v4
	v_div_fmas_f32 v4, v4, v8, v5
	v_div_fixup_f32 v8, v4, v6, 1.0
	v_cmp_gt_u32_e32 vcc, 32, v41
	s_waitcnt vmcnt(1)
	v_pk_fma_f32 v[4:5], v[8:9], v[0:1], v[52:53] op_sel_hi:[0,1,1]
	s_waitcnt vmcnt(0)
	v_pk_fma_f32 v[0:1], v[8:9], v[14:15], v[56:57] op_sel_hi:[0,1,1]
	v_pk_fma_f32 v[6:7], v[8:9], v[2:3], v[54:55] op_sel_hi:[0,1,1]
	v_pk_fma_f32 v[2:3], v[8:9], v[10:11], v[58:59] op_sel_hi:[0,1,1]
	v_cvt_pk_f16_f32 v10, v4, v5
	v_cvt_pk_f16_f32 v12, v0, v1
	v_cvt_pk_f16_f32 v11, v6, v7
	v_cvt_pk_f16_f32 v13, v2, v3
	global_store_dwordx4 v[16:17], v[4:7], off
	global_store_dwordx4 v[16:17], v[0:3], off offset:16
	global_store_dwordx4 v[22:23], v[10:13], off
	s_and_b64 exec, exec, vcc
	s_cbranch_execz .LBB3_13
	s_mov_b64 s[0:1], s[14:15]
	v_lshlrev_b32_e32 v8, 3, v43
	v_lshlrev_b64 v[10:11], 8, v[24:25]
	v_lshlrev_b32_e32 v8, 2, v8
	s_waitcnt lgkmcnt(0)
	v_lshl_add_u64 v[10:11], s[0:1], 0, v[10:11]
	v_lshl_add_u64 v[8:9], v[10:11], 0, v[8:9]
	global_store_dwordx4 v[8:9], v[4:7], off
	global_store_dwordx4 v[8:9], v[0:3], off offset:16

	.amdhsa_kernel _Z6k_agg2PKDv4_jPKiS3_PK15HIP_vector_typeIiLj2EEPKfPfSA_PS_
		.amdhsa_group_segment_fixed_size 0
		.amdhsa_private_segment_fixed_size 0
		.amdhsa_kernarg_size 64
		.amdhsa_user_sgpr_count 2
		.amdhsa_user_sgpr_dispatch_ptr 0
		.amdhsa_user_sgpr_queue_ptr 0
		.amdhsa_user_sgpr_kernarg_segment_ptr 1
		.amdhsa_user_sgpr_dispatch_id 0
		.amdhsa_user_sgpr_kernarg_preload_length 0
		.amdhsa_user_sgpr_kernarg_preload_offset 0
		.amdhsa_user_sgpr_private_segment_size 0
		.amdhsa_uses_dynamic_stack 0
		.amdhsa_enable_private_segment 0
		.amdhsa_system_sgpr_workgroup_id_x 1
		.amdhsa_system_sgpr_workgroup_id_y 0
		.amdhsa_system_sgpr_workgroup_id_z 0
		.amdhsa_system_sgpr_workgroup_info 0
		.amdhsa_system_vgpr_workitem_id 0
		.amdhsa_next_free_vgpr 62
		.amdhsa_next_free_sgpr 20
		.amdhsa_accum_offset 64
		.amdhsa_reserve_vcc 1
		.amdhsa_float_round_mode_32 0
		.amdhsa_float_round_mode_16_64 0
		.amdhsa_float_denorm_mode_32 3
		.amdhsa_float_denorm_mode_16_64 3
		.amdhsa_dx10_clamp 1
		.amdhsa_ieee_mode 1
		.amdhsa_fp16_overflow 0
		.amdhsa_tg_split 0
		.amdhsa_exception_fp_ieee_invalid_op 0
		.amdhsa_exception_fp_denorm_src 0
		.amdhsa_exception_fp_ieee_div_zero 0
		.amdhsa_exception_fp_ieee_overflow 0
		.amdhsa_exception_fp_ieee_underflow 0
		.amdhsa_exception_fp_ieee_inexact 0
		.amdhsa_exception_int_div_zero 0
	.end_amdhsa_kernel

amdhsa.kernels:
  - .agpr_count:     0
    .args:
      - .actual_access:  read_only
        .address_space:  global
        .offset:         0
        .size:           8
        .value_kind:     global_buffer
      - .actual_access:  read_only
        .address_space:  global
        .offset:         8
        .size:           8
        .value_kind:     global_buffer
      - .actual_access:  read_only
        .address_space:  global
        .offset:         16
        .size:           8
        .value_kind:     global_buffer
      - .actual_access:  write_only
        .address_space:  global
        .offset:         24
        .size:           8
        .value_kind:     global_buffer
      - .actual_access:  write_only
        .address_space:  global
        .offset:         32
        .size:           8
        .value_kind:     global_buffer
      - .actual_access:  write_only
        .address_space:  global
        .offset:         40
        .size:           8
        .value_kind:     global_buffer
      - .actual_access:  read_only
        .address_space:  global
        .offset:         48
        .size:           8
        .value_kind:     global_buffer
      - .actual_access:  read_only
        .address_space:  global
        .offset:         56
        .size:           8
        .value_kind:     global_buffer
      - .actual_access:  read_only
        .address_space:  global
        .offset:         64
        .size:           8
        .value_kind:     global_buffer
      - .actual_access:  write_only
        .address_space:  global
        .offset:         72
        .size:           8
        .value_kind:     global_buffer
    .group_segment_fixed_size: 0
    .kernarg_segment_align: 8
    .kernarg_segment_size: 80
    .language:       OpenCL C
    .language_version:
      - 2
      - 0
    .max_flat_workgroup_size: 256
    .name:           _Z8k_phase1PKfS0_S0_PDv4_jS2_PiS3_P15HIP_vector_typeIiLj2EES0_Pf
    .private_segment_fixed_size: 0
    .sgpr_count:     18
    .sgpr_spill_count: 0
    .symbol:         _Z8k_phase1PKfS0_S0_PDv4_jS2_PiS3_P15HIP_vector_typeIiLj2EES0_Pf.kd
    .uniform_work_group_size: 1
    .uses_dynamic_stack: false
    .vgpr_count:     19
    .vgpr_spill_count: 0
    .wavefront_size: 64
  - .agpr_count:     0
    .args:
      - .actual_access:  read_only
        .address_space:  global
        .offset:         0
        .size:           8
        .value_kind:     global_buffer
      - .actual_access:  read_only
        .address_space:  global
        .offset:         8
        .size:           8
        .value_kind:     global_buffer
      - .actual_access:  read_only
        .address_space:  global
        .offset:         16
        .size:           8
        .value_kind:     global_buffer
      - .actual_access:  read_only
        .address_space:  global
        .offset:         24
        .size:           8
        .value_kind:     global_buffer
      - .address_space:  global
        .offset:         32
        .size:           8
        .value_kind:     global_buffer
      - .actual_access:  write_only
        .address_space:  global
        .offset:         40
        .size:           8
        .value_kind:     global_buffer
      - .actual_access:  write_only
        .address_space:  global
        .offset:         48
        .size:           8
        .value_kind:     global_buffer
      - .actual_access:  write_only
        .address_space:  global
        .offset:         56
        .size:           8
        .value_kind:     global_buffer
      - .actual_access:  read_only
        .address_space:  global
        .offset:         64
        .size:           8
        .value_kind:     global_buffer
      - .actual_access:  write_only
        .address_space:  global
        .offset:         72
        .size:           8
        .value_kind:     global_buffer
      - .actual_access:  write_only
        .address_space:  global
        .offset:         80
        .size:           8
        .value_kind:     global_buffer
    .group_segment_fixed_size: 90112
    .kernarg_segment_align: 8
    .kernarg_segment_size: 88
    .language:       OpenCL C
    .language_version:
      - 2
      - 0
    .max_flat_workgroup_size: 768
    .name:           _Z7k_gemm1PKfS0_PKDv4_jPKiPiS6_P15HIP_vector_typeIiLj2EEPDF16_S0_S6_S9_
    .private_segment_fixed_size: 0
    .sgpr_count:     48
    .sgpr_spill_count: 0
    .symbol:         _Z7k_gemm1PKfS0_PKDv4_jPKiPiS6_P15HIP_vector_typeIiLj2EEPDF16_S0_S6_S9_.kd
    .uniform_work_group_size: 1
    .uses_dynamic_stack: false
    .vgpr_count:     168
    .vgpr_spill_count: 0
    .wavefront_size: 64
  - .agpr_count:     0
    .args:
      - .actual_access:  read_only
        .address_space:  global
        .offset:         0
        .size:           8
        .value_kind:     global_buffer
      - .actual_access:  read_only
        .address_space:  global
        .offset:         8
        .size:           8
        .value_kind:     global_buffer
      - .actual_access:  read_only
        .address_space:  global
        .offset:         16
        .size:           8
        .value_kind:     global_buffer
      - .actual_access:  read_only
        .address_space:  global
        .offset:         24
        .size:           8
        .value_kind:     global_buffer
      - .actual_access:  read_only
        .address_space:  global
        .offset:         32
        .size:           8
        .value_kind:     global_buffer
      - .actual_access:  read_only
        .address_space:  global
        .offset:         40
        .size:           8
        .value_kind:     global_buffer
      - .actual_access:  write_only
        .address_space:  global
        .offset:         48
        .size:           8
        .value_kind:     global_buffer
    .group_segment_fixed_size: 12576
    .kernarg_segment_align: 8
    .kernarg_segment_size: 56
    .language:       OpenCL C
    .language_version:
      - 2
      - 0
    .max_flat_workgroup_size: 256
    .name:           _Z8k_agg1g2PKDv4_jPKiS3_PK15HIP_vector_typeIiLj2EEPKfS1_PDF16_
    .private_segment_fixed_size: 0
    .sgpr_count:     52
    .sgpr_spill_count: 0
    .symbol:         _Z8k_agg1g2PKDv4_jPKiS3_PK15HIP_vector_typeIiLj2EEPKfS1_PDF16_.kd
    .uniform_work_group_size: 1
    .uses_dynamic_stack: false
    .vgpr_count:     126
    .vgpr_spill_count: 0
    .wavefront_size: 64
  - .agpr_count:     0
    .args:
      - .actual_access:  read_only
        .address_space:  global
        .offset:         0
        .size:           8
        .value_kind:     global_buffer
      - .actual_access:  read_only
        .address_space:  global
        .offset:         8
        .size:           8
        .value_kind:     global_buffer
      - .actual_access:  read_only
        .address_space:  global
        .offset:         16
        .size:           8
        .value_kind:     global_buffer
      - .actual_access:  read_only
        .address_space:  global
        .offset:         24
        .size:           8
        .value_kind:     global_buffer
      - .actual_access:  read_only
        .address_space:  global
        .offset:         32
        .size:           8
        .value_kind:     global_buffer
      - .actual_access:  write_only
        .address_space:  global
        .offset:         40
        .size:           8
        .value_kind:     global_buffer
      - .actual_access:  write_only
        .address_space:  global
        .offset:         48
        .size:           8
        .value_kind:     global_buffer
      - .actual_access:  write_only
        .address_space:  global
        .offset:         56
        .size:           8
        .value_kind:     global_buffer
    .group_segment_fixed_size: 0
    .kernarg_segment_align: 8
    .kernarg_segment_size: 64
    .language:       OpenCL C
    .language_version:
      - 2
      - 0
    .max_flat_workgroup_size: 256
    .name:           _Z6k_agg2PKDv4_jPKiS3_PK15HIP_vector_typeIiLj2EEPKfPfSA_PS_
    .private_segment_fixed_size: 0
    .sgpr_count:     26
    .sgpr_spill_count: 0
    .symbol:         _Z6k_agg2PKDv4_jPKiS3_PK15HIP_vector_typeIiLj2EEPKfPfSA_PS_.kd
    .uniform_work_group_size: 1
    .uses_dynamic_stack: false
    .vgpr_count:     62
    .vgpr_spill_count: 0
    .wavefront_size: 64
  - .agpr_count:     0
    .args:
      - .actual_access:  read_only
        .address_space:  global
        .offset:         0
        .size:           8
        .value_kind:     global_buffer
      - .actual_access:  read_only
        .address_space:  global
        .offset:         8
        .size:           8
        .value_kind:     global_buffer
      - .actual_access:  read_only
        .address_space:  global
        .offset:         16
        .size:           8
        .value_kind:     global_buffer
      - .actual_access:  read_only
        .address_space:  global
        .offset:         24
        .size:           8
        .value_kind:     global_buffer
      - .actual_access:  read_only
        .address_space:  global
        .offset:         32
        .size:           8
        .value_kind:     global_buffer
      - .actual_access:  read_only
        .address_space:  global
        .offset:         40
        .size:           8
        .value_kind:     global_buffer
      - .actual_access:  read_only
        .address_space:  global
        .offset:         48
        .size:           8
        .value_kind:     global_buffer
      - .actual_access:  write_only
        .address_space:  global
        .offset:         56
        .size:           8
        .value_kind:     global_buffer
      - .actual_access:  write_only
        .address_space:  global
        .offset:         64
        .size:           8
        .value_kind:     global_buffer
    .group_segment_fixed_size: 6144
    .kernarg_segment_align: 8
    .kernarg_segment_size: 72
    .language:       OpenCL C
    .language_version:
      - 2
      - 0
    .max_flat_workgroup_size: 256
    .name:           _Z9k_readoutPKDv4_jPKfPKiPK15HIP_vector_typeIiLj2EES3_S3_S3_PfSA_
    .private_segment_fixed_size: 0
    .sgpr_count:     20
    .sgpr_spill_count: 0
    .symbol:         _Z9k_readoutPKDv4_jPKfPKiPK15HIP_vector_typeIiLj2EES3_S3_S3_PfSA_.kd
    .uniform_work_group_size: 1
    .uses_dynamic_stack: false
    .vgpr_count:     92
    .vgpr_spill_count: 0
    .wavefront_size: 64
